# tconv8 epilogue stores staged through wave-private LDS so every global_store_dwordx4 writes 8 rows x full 128-byte lines (ZT bf16 and Z8 fp8), one barrier after the main loop frees the filter-copy LDS
# speedup vs baseline: 1.0199x; 1.0017x over previous
.LBB0_539:
	s_add_i32 s5, s4, 0x80
	s_and_b32 s72, s5, 0xf80
	v_lshl_add_u64 v[168:169], v[188:189], 0, s[72:73]
	global_load_dwordx4 v[172:175], v[168:169], off
	s_nop 0
	global_load_dwordx4 v[168:171], v[168:169], off offset:16
	v_add_u32_e32 v185, s4, v192
	v_add_u32_e32 v203, s72, v192
	ds_read_b128 v[204:207], v185 offset:320
	ds_read_b128 v[208:211], v185 offset:336
	ds_read_b128 v[212:215], v185 offset:352
	ds_read_b128 v[216:219], v185 offset:368
	ds_read_b128 v[220:223], v185 offset:384
	ds_read_b128 v[224:227], v185 offset:400
	ds_read_b128 v[228:231], v185 offset:416
	s_waitcnt vmcnt(2) lgkmcnt(7)
	v_mfma_f32_16x16x128_f8f6f4 v[164:167], v[28:35], v[0:7], v[164:167]
	v_mfma_f32_16x16x128_f8f6f4 v[160:163], v[24:31], v[0:7], v[160:163]
	v_mfma_f32_16x16x128_f8f6f4 v[156:159], v[20:27], v[0:7], v[156:159]
	v_mfma_f32_16x16x128_f8f6f4 v[152:155], v[16:23], v[0:7], v[152:155]
	v_mfma_f32_16x16x128_f8f6f4 v[148:151], v[12:19], v[0:7], v[148:151]
	v_mfma_f32_16x16x128_f8f6f4 v[144:147], v[8:15], v[0:7], v[144:147]
	ds_read_b128 v[8:11], v185 offset:240
	ds_read_b128 v[12:15], v185 offset:256
	ds_read_b128 v[16:19], v185 offset:272
	ds_read_b128 v[20:23], v185 offset:288
	ds_read_b128 v[24:27], v185 offset:304
	ds_read_b128 v[28:31], v185 offset:320
	s_waitcnt lgkmcnt(6)
	v_mfma_f32_16x16x128_f8f6f4 v[140:143], v[224:231], v[0:7], v[140:143]
	v_mfma_f32_16x16x128_f8f6f4 v[136:139], v[220:227], v[0:7], v[136:139]
	v_mfma_f32_16x16x128_f8f6f4 v[132:135], v[216:223], v[0:7], v[132:135]
	v_mfma_f32_16x16x128_f8f6f4 v[128:131], v[212:219], v[0:7], v[128:131]
	v_mfma_f32_16x16x128_f8f6f4 v[124:127], v[208:215], v[0:7], v[124:127]
	v_mfma_f32_16x16x128_f8f6f4 v[120:123], v[204:211], v[0:7], v[120:123]
	ds_read_b128 v[204:207], v185 offset:160
	ds_read_b128 v[208:211], v185 offset:176
	ds_read_b128 v[212:215], v185 offset:192
	ds_read_b128 v[216:219], v185 offset:208
	ds_read_b128 v[220:223], v185 offset:224
	ds_read_b128 v[224:227], v185 offset:240
	s_waitcnt lgkmcnt(6)
	v_mfma_f32_16x16x128_f8f6f4 v[116:119], v[24:31], v[0:7], v[116:119]
	v_mfma_f32_16x16x128_f8f6f4 v[112:115], v[20:27], v[0:7], v[112:115]
	v_mfma_f32_16x16x128_f8f6f4 v[108:111], v[16:23], v[0:7], v[108:111]
	v_mfma_f32_16x16x128_f8f6f4 v[104:107], v[12:19], v[0:7], v[104:107]
	v_mfma_f32_16x16x128_f8f6f4 v[100:103], v[8:15], v[0:7], v[100:103]
	ds_read_b128 v[8:11], v185 offset:80
	ds_read_b128 v[12:15], v185 offset:96
	ds_read_b128 v[16:19], v185 offset:112
	ds_read_b128 v[20:23], v185 offset:128
	ds_read_b128 v[24:27], v185 offset:144
	ds_read_b128 v[28:31], v185 offset:160
	s_waitcnt lgkmcnt(6)
	v_mfma_f32_16x16x128_f8f6f4 v[96:99], v[220:227], v[0:7], v[96:99]
	v_mfma_f32_16x16x128_f8f6f4 v[92:95], v[216:223], v[0:7], v[92:95]
	v_mfma_f32_16x16x128_f8f6f4 v[88:91], v[212:219], v[0:7], v[88:91]
	v_mfma_f32_16x16x128_f8f6f4 v[84:87], v[208:215], v[0:7], v[84:87]
	v_mfma_f32_16x16x128_f8f6f4 v[80:83], v[204:211], v[0:7], v[80:83]
	ds_read_b128 v[204:207], v185 offset:0
	ds_read_b128 v[208:211], v185 offset:16
	ds_read_b128 v[212:215], v185 offset:32
	ds_read_b128 v[216:219], v185 offset:48
	ds_read_b128 v[220:223], v185 offset:64
	ds_read_b128 v[224:227], v185 offset:80
	s_waitcnt lgkmcnt(6)
	v_mfma_f32_16x16x128_f8f6f4 v[76:79], v[24:31], v[0:7], v[76:79]
	v_mfma_f32_16x16x128_f8f6f4 v[72:75], v[20:27], v[0:7], v[72:75]
	v_mfma_f32_16x16x128_f8f6f4 v[68:71], v[16:23], v[0:7], v[68:71]
	v_mfma_f32_16x16x128_f8f6f4 v[64:67], v[12:19], v[0:7], v[64:67]
	v_mfma_f32_16x16x128_f8f6f4 v[60:63], v[8:15], v[0:7], v[60:63]
	ds_read_b128 v[8:11], v203 offset:416
	ds_read_b128 v[12:15], v203 offset:432
	ds_read_b128 v[16:19], v203 offset:448
	ds_read_b128 v[20:23], v203 offset:464
	ds_read_b128 v[24:27], v203 offset:480
	ds_read_b128 v[28:31], v203 offset:496
	ds_read_b128 v[32:35], v203 offset:512
	s_waitcnt lgkmcnt(7)
	v_mfma_f32_16x16x128_f8f6f4 v[56:59], v[220:227], v[0:7], v[56:59]
	v_mfma_f32_16x16x128_f8f6f4 v[52:55], v[216:223], v[0:7], v[52:55]
	v_mfma_f32_16x16x128_f8f6f4 v[48:51], v[212:219], v[0:7], v[48:51]
	v_mfma_f32_16x16x128_f8f6f4 v[44:47], v[208:215], v[0:7], v[44:47]
	v_mfma_f32_16x16x128_f8f6f4 v[40:43], v[204:211], v[0:7], v[40:43]
	s_cmpk_eq_i32 s5, 0x1000
	s_mov_b32 s4, s5
	s_waitcnt vmcnt(0)
	v_mov_b32_e32 v0, v172
	v_mov_b32_e32 v1, v173
	v_mov_b32_e32 v2, v174
	v_mov_b32_e32 v3, v175
	v_mov_b32_e32 v4, v168
	v_mov_b32_e32 v5, v169
	v_mov_b32_e32 v6, v170
	v_mov_b32_e32 v7, v171
	s_cbranch_scc0 .LBB0_539
	s_waitcnt lgkmcnt(0)
	s_barrier
	s_lshl_b64 s[4:5], s[36:37], 2
	s_add_u32 s4, s31, s4
	s_addc_u32 s5, s46, s5
	global_load_dword v4, v245, s[4:5]
	v_lshl_add_u64 v[0:1], v[186:187], 0, v[182:183]
	v_lshlrev_b64 v[2:3], 1, v[0:1]
	v_lshl_add_u64 v[8:9], s[22:23], 0, v[2:3]
	v_lshl_add_u64 v[6:7], s[24:25], 0, v[2:3]
	global_load_dwordx2 v[204:205], v[8:9], off
	global_load_dwordx2 v[206:207], v[6:7], off
	global_load_dwordx2 v[208:209], v[8:9], off offset:32
	global_load_dwordx2 v[210:211], v[6:7], off offset:32
	global_load_dwordx2 v[212:213], v[8:9], off offset:64
	global_load_dwordx2 v[214:215], v[6:7], off offset:64
	global_load_dwordx2 v[216:217], v[8:9], off offset:96
	global_load_dwordx2 v[218:219], v[6:7], off offset:96
	global_load_dwordx2 v[220:221], v[8:9], off offset:128
	global_load_dwordx2 v[222:223], v[6:7], off offset:128
	global_load_dwordx2 v[224:225], v[8:9], off offset:160
	global_load_dwordx2 v[226:227], v[6:7], off offset:160
	global_load_dwordx2 v[228:229], v[8:9], off offset:192
	global_load_dwordx2 v[230:231], v[6:7], off offset:192
	global_load_dwordx2 v[232:233], v[8:9], off offset:224
	global_load_dwordx2 v[234:235], v[6:7], off offset:224
	global_load_dwordx2 v[10:11], v[8:9], off offset:256
	global_load_dwordx2 v[12:13], v[6:7], off offset:256
	global_load_dwordx2 v[14:15], v[8:9], off offset:288
	global_load_dwordx2 v[16:17], v[6:7], off offset:288
	global_load_dwordx2 v[18:19], v[8:9], off offset:320
	global_load_dwordx2 v[20:21], v[6:7], off offset:320
	global_load_dwordx2 v[22:23], v[8:9], off offset:352
	global_load_dwordx2 v[24:25], v[6:7], off offset:352
	global_load_dwordx2 v[26:27], v[8:9], off offset:384
	global_load_dwordx2 v[28:29], v[6:7], off offset:384
	global_load_dwordx2 v[30:31], v[8:9], off offset:416
	global_load_dwordx2 v[32:33], v[6:7], off offset:416
	global_load_dwordx2 v[34:35], v[8:9], off offset:448
	global_load_dwordx2 v[36:37], v[6:7], off offset:448
	global_load_dwordx2 v[236:237], v[8:9], off offset:480
	global_load_dwordx2 v[238:239], v[6:7], off offset:480
	v_lshl_add_u64 v[2:3], s[26:27], 0, v[2:3]
	v_lshl_add_u64 v[0:1], s[28:29], 0, v[0:1]
	v_mbcnt_lo_u32_b32 v5, -1, 0
	v_mbcnt_hi_u32_b32 v5, -1, v5
	v_and_b32_e32 v38, 15, v5
	v_lshrrev_b32_e32 v39, 4, v5
	v_lshrrev_b32_e32 v246, 3, v5
	v_and_b32_e32 v247, 7, v5
	v_sub_u32_e32 v248, v246, v38
	v_mul_i32_i24_e32 v249, 0x600000, v248
	v_lshlrev_b32_e32 v250, 3, v39
	v_sub_u32_e32 v249, v249, v250
	v_lshlrev_b32_e32 v251, 4, v247
	v_add_u32_e32 v198, v249, v251
	v_ashrrev_i32_e32 v199, 31, v198
	v_lshl_add_u64 v[194:195], v[198:199], 0, v[2:3]
	v_mov_b32_e32 v198, 0x3000000
	v_mov_b32_e32 v199, 0
	v_lshl_add_u64 v[196:197], v[198:199], 0, v[194:195]
	v_mul_i32_i24_e32 v249, 0x300000, v248
	v_lshlrev_b32_e32 v250, 2, v39
	v_sub_u32_e32 v249, v249, v250
	v_add_u32_e32 v198, v249, v251
	v_ashrrev_i32_e32 v199, 31, v198
	v_lshl_add_u64 v[2:3], v[198:199], 0, v[0:1]
	v_mov_b32_e32 v198, 0x1800000
	v_mov_b32_e32 v199, 0
	v_lshl_add_u64 v[198:199], v[198:199], 0, v[2:3]
	v_lshrrev_b32_e32 v250, 6, v200
	v_mul_u32_u24_e32 v250, 0x1200, v250
	v_mul_u32_u24_e32 v249, 0x90, v38
	v_add_u32_e32 v249, v249, v250
	v_lshl_add_u32 v0, v39, 3, v249
	v_lshl_add_u32 v248, v39, 2, v249
	v_add_u32_e32 v248, 0x900, v248
	v_mul_u32_u24_e32 v246, 0x90, v246
	v_add_u32_e32 v246, v246, v250
	v_add_u32_e32 v1, v246, v251
	v_mov_b32_e32 v38, v248
	v_add_u32_e32 v39, 0x900, v1
	v_mov_b32_e32 v252, 0x43dc0000
	s_and_b64 vcc, exec, s[34:35]
	s_waitcnt vmcnt(16)
	v_lshlrev_b32_e32 v168, 16, v204
	v_and_b32_e32 v169, 0xffff0000, v204
	v_lshlrev_b32_e32 v170, 16, v205
	v_and_b32_e32 v171, 0xffff0000, v205
	v_lshlrev_b32_e32 v172, 16, v206
	v_and_b32_e32 v173, 0xffff0000, v206
	v_lshlrev_b32_e32 v174, 16, v207
	v_and_b32_e32 v175, 0xffff0000, v207
	v_pk_mul_f32 v[168:169], v[4:5], v[168:169] op_sel_hi:[0,1]
	v_pk_mul_f32 v[170:171], v[4:5], v[170:171] op_sel_hi:[0,1]
	v_pk_fma_f32 v[164:165], v[184:185], v[164:165], v[168:169] op_sel_hi:[0,1,1]
	v_pk_fma_f32 v[166:167], v[184:185], v[166:167], v[170:171] op_sel_hi:[0,1,1]
	v_pk_mul_f32 v[164:165], v[164:165], v[172:173]
	v_pk_mul_f32 v[166:167], v[166:167], v[174:175]
	v_cvt_pk_bf16_f32 v240, v164, v165
	v_cvt_pk_bf16_f32 v241, v166, v167
	ds_write_b64 v0, v[240:241]
	v_lshlrev_b32_e32 v168, 16, v208
	v_and_b32_e32 v169, 0xffff0000, v208
	v_lshlrev_b32_e32 v170, 16, v209
	v_and_b32_e32 v171, 0xffff0000, v209
	v_lshlrev_b32_e32 v172, 16, v210
	v_and_b32_e32 v173, 0xffff0000, v210
	v_lshlrev_b32_e32 v174, 16, v211
	v_and_b32_e32 v175, 0xffff0000, v211
	v_pk_mul_f32 v[168:169], v[4:5], v[168:169] op_sel_hi:[0,1]
	v_pk_mul_f32 v[170:171], v[4:5], v[170:171] op_sel_hi:[0,1]
	v_pk_fma_f32 v[160:161], v[184:185], v[160:161], v[168:169] op_sel_hi:[0,1,1]
	v_pk_fma_f32 v[162:163], v[184:185], v[162:163], v[170:171] op_sel_hi:[0,1,1]
	v_pk_mul_f32 v[160:161], v[160:161], v[172:173]
	v_pk_mul_f32 v[162:163], v[162:163], v[174:175]
	v_cvt_pk_bf16_f32 v240, v160, v161
	v_cvt_pk_bf16_f32 v241, v162, v163
	ds_write_b64 v0, v[240:241] offset:32
	v_lshlrev_b32_e32 v168, 16, v212
	v_and_b32_e32 v169, 0xffff0000, v212
	v_lshlrev_b32_e32 v170, 16, v213
	v_and_b32_e32 v171, 0xffff0000, v213
	v_lshlrev_b32_e32 v172, 16, v214
	v_and_b32_e32 v173, 0xffff0000, v214
	v_lshlrev_b32_e32 v174, 16, v215
	v_and_b32_e32 v175, 0xffff0000, v215
	v_pk_mul_f32 v[168:169], v[4:5], v[168:169] op_sel_hi:[0,1]
	v_pk_mul_f32 v[170:171], v[4:5], v[170:171] op_sel_hi:[0,1]
	v_pk_fma_f32 v[156:157], v[184:185], v[156:157], v[168:169] op_sel_hi:[0,1,1]
	v_pk_fma_f32 v[158:159], v[184:185], v[158:159], v[170:171] op_sel_hi:[0,1,1]
	v_pk_mul_f32 v[156:157], v[156:157], v[172:173]
	v_pk_mul_f32 v[158:159], v[158:159], v[174:175]
	v_cvt_pk_bf16_f32 v240, v156, v157
	v_cvt_pk_bf16_f32 v241, v158, v159
	ds_write_b64 v0, v[240:241] offset:64
	v_lshlrev_b32_e32 v168, 16, v216
	v_and_b32_e32 v169, 0xffff0000, v216
	v_lshlrev_b32_e32 v170, 16, v217
	v_and_b32_e32 v171, 0xffff0000, v217
	v_lshlrev_b32_e32 v172, 16, v218
	v_and_b32_e32 v173, 0xffff0000, v218
	v_lshlrev_b32_e32 v174, 16, v219
	v_and_b32_e32 v175, 0xffff0000, v219
	v_pk_mul_f32 v[168:169], v[4:5], v[168:169] op_sel_hi:[0,1]
	v_pk_mul_f32 v[170:171], v[4:5], v[170:171] op_sel_hi:[0,1]
	v_pk_fma_f32 v[152:153], v[184:185], v[152:153], v[168:169] op_sel_hi:[0,1,1]
	v_pk_fma_f32 v[154:155], v[184:185], v[154:155], v[170:171] op_sel_hi:[0,1,1]
	v_pk_mul_f32 v[152:153], v[152:153], v[172:173]
	v_pk_mul_f32 v[154:155], v[154:155], v[174:175]
	v_cvt_pk_bf16_f32 v240, v152, v153
	v_cvt_pk_bf16_f32 v241, v154, v155
	ds_write_b64 v0, v[240:241] offset:96
	ds_read_b128 v[168:171], v1
	ds_read_b128 v[172:175], v1 offset:1152
	s_cbranch_vccz .Lt8z_0_0
	v_med3_f32 v248, v164, s77, v252
	v_med3_f32 v249, v165, s77, v252
	v_med3_f32 v250, v166, s77, v252
	v_med3_f32 v251, v167, s77, v252
	v_mov_b32_e32 v246, v245
	v_cvt_pk_fp8_f32 v246, v248, v249
	v_cvt_pk_fp8_f32 v246, v250, v251 op_sel:[0,0,1]
	ds_write_b32 v38, v246
	v_med3_f32 v248, v160, s77, v252
	v_med3_f32 v249, v161, s77, v252
	v_med3_f32 v250, v162, s77, v252
	v_med3_f32 v251, v163, s77, v252
	v_mov_b32_e32 v246, v245
	v_cvt_pk_fp8_f32 v246, v248, v249
	v_cvt_pk_fp8_f32 v246, v250, v251 op_sel:[0,0,1]
	ds_write_b32 v38, v246 offset:16
	v_med3_f32 v248, v156, s77, v252
	v_med3_f32 v249, v157, s77, v252
	v_med3_f32 v250, v158, s77, v252
	v_med3_f32 v251, v159, s77, v252
	v_mov_b32_e32 v246, v245
	v_cvt_pk_fp8_f32 v246, v248, v249
	v_cvt_pk_fp8_f32 v246, v250, v251 op_sel:[0,0,1]
	ds_write_b32 v38, v246 offset:32
	v_med3_f32 v248, v152, s77, v252
	v_med3_f32 v249, v153, s77, v252
	v_med3_f32 v250, v154, s77, v252
	v_med3_f32 v251, v155, s77, v252
	v_mov_b32_e32 v246, v245
	v_cvt_pk_fp8_f32 v246, v248, v249
	v_cvt_pk_fp8_f32 v246, v250, v251 op_sel:[0,0,1]
	ds_write_b32 v38, v246 offset:48
.Lt8z_0_0:
	s_waitcnt lgkmcnt(0)
	global_store_dwordx4 v[194:195], v[168:171], off
	global_store_dwordx4 v[196:197], v[172:175], off
	s_nop 1
	v_lshlrev_b32_e32 v168, 16, v220
	v_and_b32_e32 v169, 0xffff0000, v220
	v_lshlrev_b32_e32 v170, 16, v221
	v_and_b32_e32 v171, 0xffff0000, v221
	v_lshlrev_b32_e32 v172, 16, v222
	v_and_b32_e32 v173, 0xffff0000, v222
	v_lshlrev_b32_e32 v174, 16, v223
	v_and_b32_e32 v175, 0xffff0000, v223
	v_pk_mul_f32 v[168:169], v[4:5], v[168:169] op_sel_hi:[0,1]
	v_pk_mul_f32 v[170:171], v[4:5], v[170:171] op_sel_hi:[0,1]
	v_pk_fma_f32 v[148:149], v[184:185], v[148:149], v[168:169] op_sel_hi:[0,1,1]
	v_pk_fma_f32 v[150:151], v[184:185], v[150:151], v[170:171] op_sel_hi:[0,1,1]
	v_pk_mul_f32 v[148:149], v[148:149], v[172:173]
	v_pk_mul_f32 v[150:151], v[150:151], v[174:175]
	v_cvt_pk_bf16_f32 v240, v148, v149
	v_cvt_pk_bf16_f32 v241, v150, v151
	ds_write_b64 v0, v[240:241]
	v_lshlrev_b32_e32 v168, 16, v224
	v_and_b32_e32 v169, 0xffff0000, v224
	v_lshlrev_b32_e32 v170, 16, v225
	v_and_b32_e32 v171, 0xffff0000, v225
	v_lshlrev_b32_e32 v172, 16, v226
	v_and_b32_e32 v173, 0xffff0000, v226
	v_lshlrev_b32_e32 v174, 16, v227
	v_and_b32_e32 v175, 0xffff0000, v227
	v_pk_mul_f32 v[168:169], v[4:5], v[168:169] op_sel_hi:[0,1]
	v_pk_mul_f32 v[170:171], v[4:5], v[170:171] op_sel_hi:[0,1]
	v_pk_fma_f32 v[144:145], v[184:185], v[144:145], v[168:169] op_sel_hi:[0,1,1]
	v_pk_fma_f32 v[146:147], v[184:185], v[146:147], v[170:171] op_sel_hi:[0,1,1]
	v_pk_mul_f32 v[144:145], v[144:145], v[172:173]
	v_pk_mul_f32 v[146:147], v[146:147], v[174:175]
	v_cvt_pk_bf16_f32 v240, v144, v145
	v_cvt_pk_bf16_f32 v241, v146, v147
	ds_write_b64 v0, v[240:241] offset:32
	v_lshlrev_b32_e32 v168, 16, v228
	v_and_b32_e32 v169, 0xffff0000, v228
	v_lshlrev_b32_e32 v170, 16, v229
	v_and_b32_e32 v171, 0xffff0000, v229
	v_lshlrev_b32_e32 v172, 16, v230
	v_and_b32_e32 v173, 0xffff0000, v230
	v_lshlrev_b32_e32 v174, 16, v231
	v_and_b32_e32 v175, 0xffff0000, v231
	v_pk_mul_f32 v[168:169], v[4:5], v[168:169] op_sel_hi:[0,1]
	v_pk_mul_f32 v[170:171], v[4:5], v[170:171] op_sel_hi:[0,1]
	v_pk_fma_f32 v[140:141], v[184:185], v[140:141], v[168:169] op_sel_hi:[0,1,1]
	v_pk_fma_f32 v[142:143], v[184:185], v[142:143], v[170:171] op_sel_hi:[0,1,1]
	v_pk_mul_f32 v[140:141], v[140:141], v[172:173]
	v_pk_mul_f32 v[142:143], v[142:143], v[174:175]
	v_cvt_pk_bf16_f32 v240, v140, v141
	v_cvt_pk_bf16_f32 v241, v142, v143
	ds_write_b64 v0, v[240:241] offset:64
	v_lshlrev_b32_e32 v168, 16, v232
	v_and_b32_e32 v169, 0xffff0000, v232
	v_lshlrev_b32_e32 v170, 16, v233
	v_and_b32_e32 v171, 0xffff0000, v233
	v_lshlrev_b32_e32 v172, 16, v234
	v_and_b32_e32 v173, 0xffff0000, v234
	v_lshlrev_b32_e32 v174, 16, v235
	v_and_b32_e32 v175, 0xffff0000, v235
	v_pk_mul_f32 v[168:169], v[4:5], v[168:169] op_sel_hi:[0,1]
	v_pk_mul_f32 v[170:171], v[4:5], v[170:171] op_sel_hi:[0,1]
	v_pk_fma_f32 v[136:137], v[184:185], v[136:137], v[168:169] op_sel_hi:[0,1,1]
	v_pk_fma_f32 v[138:139], v[184:185], v[138:139], v[170:171] op_sel_hi:[0,1,1]
	v_pk_mul_f32 v[136:137], v[136:137], v[172:173]
	v_pk_mul_f32 v[138:139], v[138:139], v[174:175]
	v_cvt_pk_bf16_f32 v240, v136, v137
	v_cvt_pk_bf16_f32 v241, v138, v139
	ds_write_b64 v0, v[240:241] offset:96
	ds_read_b128 v[168:171], v1
	ds_read_b128 v[172:175], v1 offset:1152
	s_cbranch_vccz .Lt8z_0_1
	v_med3_f32 v248, v148, s77, v252
	v_med3_f32 v249, v149, s77, v252
	v_med3_f32 v250, v150, s77, v252
	v_med3_f32 v251, v151, s77, v252
	v_mov_b32_e32 v246, v245
	v_cvt_pk_fp8_f32 v246, v248, v249
	v_cvt_pk_fp8_f32 v246, v250, v251 op_sel:[0,0,1]
	ds_write_b32 v38, v246 offset:64
	v_med3_f32 v248, v144, s77, v252
	v_med3_f32 v249, v145, s77, v252
	v_med3_f32 v250, v146, s77, v252
	v_med3_f32 v251, v147, s77, v252
	v_mov_b32_e32 v246, v245
	v_cvt_pk_fp8_f32 v246, v248, v249
	v_cvt_pk_fp8_f32 v246, v250, v251 op_sel:[0,0,1]
	ds_write_b32 v38, v246 offset:80
	v_med3_f32 v248, v140, s77, v252
	v_med3_f32 v249, v141, s77, v252
	v_med3_f32 v250, v142, s77, v252
	v_med3_f32 v251, v143, s77, v252
	v_mov_b32_e32 v246, v245
	v_cvt_pk_fp8_f32 v246, v248, v249
	v_cvt_pk_fp8_f32 v246, v250, v251 op_sel:[0,0,1]
	ds_write_b32 v38, v246 offset:96
	v_med3_f32 v248, v136, s77, v252
	v_med3_f32 v249, v137, s77, v252
	v_med3_f32 v250, v138, s77, v252
	v_med3_f32 v251, v139, s77, v252
	v_mov_b32_e32 v246, v245
	v_cvt_pk_fp8_f32 v246, v248, v249
	v_cvt_pk_fp8_f32 v246, v250, v251 op_sel:[0,0,1]
	ds_write_b32 v38, v246 offset:112
.Lt8z_0_1:
	s_waitcnt lgkmcnt(0)
	global_store_dwordx4 v[194:195], v[168:171], off offset:128
	global_store_dwordx4 v[196:197], v[172:175], off offset:128
	s_nop 1
	s_cbranch_vccz .Lt8zs_0
	ds_read_b128 v[168:171], v39
	ds_read_b128 v[172:175], v39 offset:1152
	s_waitcnt lgkmcnt(0)
	global_store_dwordx4 v[2:3], v[168:171], off
	global_store_dwordx4 v[198:199], v[172:175], off
	s_nop 1
.Lt8zs_0:
	global_load_dwordx2 v[204:205], v[8:9], off offset:512
	global_load_dwordx2 v[206:207], v[6:7], off offset:512
	global_load_dwordx2 v[208:209], v[8:9], off offset:544
	global_load_dwordx2 v[210:211], v[6:7], off offset:544
	global_load_dwordx2 v[212:213], v[8:9], off offset:576
	global_load_dwordx2 v[214:215], v[6:7], off offset:576
	global_load_dwordx2 v[216:217], v[8:9], off offset:608
	global_load_dwordx2 v[218:219], v[6:7], off offset:608
	global_load_dwordx2 v[220:221], v[8:9], off offset:640
	global_load_dwordx2 v[222:223], v[6:7], off offset:640
	global_load_dwordx2 v[224:225], v[8:9], off offset:672
	global_load_dwordx2 v[226:227], v[6:7], off offset:672
	global_load_dwordx2 v[228:229], v[8:9], off offset:704
	global_load_dwordx2 v[230:231], v[6:7], off offset:704
	global_load_dwordx2 v[232:233], v[8:9], off offset:736
	global_load_dwordx2 v[234:235], v[6:7], off offset:736
	s_waitcnt vmcnt(20)
	v_lshlrev_b32_e32 v168, 16, v10
	v_and_b32_e32 v169, 0xffff0000, v10
	v_lshlrev_b32_e32 v170, 16, v11
	v_and_b32_e32 v171, 0xffff0000, v11
	v_lshlrev_b32_e32 v172, 16, v12
	v_and_b32_e32 v173, 0xffff0000, v12
	v_lshlrev_b32_e32 v174, 16, v13
	v_and_b32_e32 v175, 0xffff0000, v13
	v_pk_mul_f32 v[168:169], v[4:5], v[168:169] op_sel_hi:[0,1]
	v_pk_mul_f32 v[170:171], v[4:5], v[170:171] op_sel_hi:[0,1]
	v_pk_fma_f32 v[132:133], v[184:185], v[132:133], v[168:169] op_sel_hi:[0,1,1]
	v_pk_fma_f32 v[134:135], v[184:185], v[134:135], v[170:171] op_sel_hi:[0,1,1]
	v_pk_mul_f32 v[132:133], v[132:133], v[172:173]
	v_pk_mul_f32 v[134:135], v[134:135], v[174:175]
	v_cvt_pk_bf16_f32 v240, v132, v133
	v_cvt_pk_bf16_f32 v241, v134, v135
	ds_write_b64 v0, v[240:241]
	v_lshlrev_b32_e32 v168, 16, v14
	v_and_b32_e32 v169, 0xffff0000, v14
	v_lshlrev_b32_e32 v170, 16, v15
	v_and_b32_e32 v171, 0xffff0000, v15
	v_lshlrev_b32_e32 v172, 16, v16
	v_and_b32_e32 v173, 0xffff0000, v16
	v_lshlrev_b32_e32 v174, 16, v17
	v_and_b32_e32 v175, 0xffff0000, v17
	v_pk_mul_f32 v[168:169], v[4:5], v[168:169] op_sel_hi:[0,1]
	v_pk_mul_f32 v[170:171], v[4:5], v[170:171] op_sel_hi:[0,1]
	v_pk_fma_f32 v[128:129], v[184:185], v[128:129], v[168:169] op_sel_hi:[0,1,1]
	v_pk_fma_f32 v[130:131], v[184:185], v[130:131], v[170:171] op_sel_hi:[0,1,1]
	v_pk_mul_f32 v[128:129], v[128:129], v[172:173]
	v_pk_mul_f32 v[130:131], v[130:131], v[174:175]
	v_cvt_pk_bf16_f32 v240, v128, v129
	v_cvt_pk_bf16_f32 v241, v130, v131
	ds_write_b64 v0, v[240:241] offset:32
	v_lshlrev_b32_e32 v168, 16, v18
	v_and_b32_e32 v169, 0xffff0000, v18
	v_lshlrev_b32_e32 v170, 16, v19
	v_and_b32_e32 v171, 0xffff0000, v19
	v_lshlrev_b32_e32 v172, 16, v20
	v_and_b32_e32 v173, 0xffff0000, v20
	v_lshlrev_b32_e32 v174, 16, v21
	v_and_b32_e32 v175, 0xffff0000, v21
	v_pk_mul_f32 v[168:169], v[4:5], v[168:169] op_sel_hi:[0,1]
	v_pk_mul_f32 v[170:171], v[4:5], v[170:171] op_sel_hi:[0,1]
	v_pk_fma_f32 v[124:125], v[184:185], v[124:125], v[168:169] op_sel_hi:[0,1,1]
	v_pk_fma_f32 v[126:127], v[184:185], v[126:127], v[170:171] op_sel_hi:[0,1,1]
	v_pk_mul_f32 v[124:125], v[124:125], v[172:173]
	v_pk_mul_f32 v[126:127], v[126:127], v[174:175]
	v_cvt_pk_bf16_f32 v240, v124, v125
	v_cvt_pk_bf16_f32 v241, v126, v127
	ds_write_b64 v0, v[240:241] offset:64
	v_lshlrev_b32_e32 v168, 16, v22
	v_and_b32_e32 v169, 0xffff0000, v22
	v_lshlrev_b32_e32 v170, 16, v23
	v_and_b32_e32 v171, 0xffff0000, v23
	v_lshlrev_b32_e32 v172, 16, v24
	v_and_b32_e32 v173, 0xffff0000, v24
	v_lshlrev_b32_e32 v174, 16, v25
	v_and_b32_e32 v175, 0xffff0000, v25
	v_pk_mul_f32 v[168:169], v[4:5], v[168:169] op_sel_hi:[0,1]
	v_pk_mul_f32 v[170:171], v[4:5], v[170:171] op_sel_hi:[0,1]
	v_pk_fma_f32 v[120:121], v[184:185], v[120:121], v[168:169] op_sel_hi:[0,1,1]
	v_pk_fma_f32 v[122:123], v[184:185], v[122:123], v[170:171] op_sel_hi:[0,1,1]
	v_pk_mul_f32 v[120:121], v[120:121], v[172:173]
	v_pk_mul_f32 v[122:123], v[122:123], v[174:175]
	v_cvt_pk_bf16_f32 v240, v120, v121
	v_cvt_pk_bf16_f32 v241, v122, v123
	ds_write_b64 v0, v[240:241] offset:96
	ds_read_b128 v[168:171], v1
	ds_read_b128 v[172:175], v1 offset:1152
	s_cbranch_vccz .Lt8z_1_0
	v_med3_f32 v248, v132, s77, v252
	v_med3_f32 v249, v133, s77, v252
	v_med3_f32 v250, v134, s77, v252
	v_med3_f32 v251, v135, s77, v252
	v_mov_b32_e32 v246, v245
	v_cvt_pk_fp8_f32 v246, v248, v249
	v_cvt_pk_fp8_f32 v246, v250, v251 op_sel:[0,0,1]
	ds_write_b32 v38, v246
	v_med3_f32 v248, v128, s77, v252
	v_med3_f32 v249, v129, s77, v252
	v_med3_f32 v250, v130, s77, v252
	v_med3_f32 v251, v131, s77, v252
	v_mov_b32_e32 v246, v245
	v_cvt_pk_fp8_f32 v246, v248, v249
	v_cvt_pk_fp8_f32 v246, v250, v251 op_sel:[0,0,1]
	ds_write_b32 v38, v246 offset:16
	v_med3_f32 v248, v124, s77, v252
	v_med3_f32 v249, v125, s77, v252
	v_med3_f32 v250, v126, s77, v252
	v_med3_f32 v251, v127, s77, v252
	v_mov_b32_e32 v246, v245
	v_cvt_pk_fp8_f32 v246, v248, v249
	v_cvt_pk_fp8_f32 v246, v250, v251 op_sel:[0,0,1]
	ds_write_b32 v38, v246 offset:32
	v_med3_f32 v248, v120, s77, v252
	v_med3_f32 v249, v121, s77, v252
	v_med3_f32 v250, v122, s77, v252
	v_med3_f32 v251, v123, s77, v252
	v_mov_b32_e32 v246, v245
	v_cvt_pk_fp8_f32 v246, v248, v249
	v_cvt_pk_fp8_f32 v246, v250, v251 op_sel:[0,0,1]
	ds_write_b32 v38, v246 offset:48
.Lt8z_1_0:
	s_waitcnt lgkmcnt(0)
	global_store_dwordx4 v[194:195], v[168:171], off offset:256
	global_store_dwordx4 v[196:197], v[172:175], off offset:256
	s_nop 1
	v_lshlrev_b32_e32 v168, 16, v26
	v_and_b32_e32 v169, 0xffff0000, v26
	v_lshlrev_b32_e32 v170, 16, v27
	v_and_b32_e32 v171, 0xffff0000, v27
	v_lshlrev_b32_e32 v172, 16, v28
	v_and_b32_e32 v173, 0xffff0000, v28
	v_lshlrev_b32_e32 v174, 16, v29
	v_and_b32_e32 v175, 0xffff0000, v29
	v_pk_mul_f32 v[168:169], v[4:5], v[168:169] op_sel_hi:[0,1]
	v_pk_mul_f32 v[170:171], v[4:5], v[170:171] op_sel_hi:[0,1]
	v_pk_fma_f32 v[116:117], v[184:185], v[116:117], v[168:169] op_sel_hi:[0,1,1]
	v_pk_fma_f32 v[118:119], v[184:185], v[118:119], v[170:171] op_sel_hi:[0,1,1]
	v_pk_mul_f32 v[116:117], v[116:117], v[172:173]
	v_pk_mul_f32 v[118:119], v[118:119], v[174:175]
	v_cvt_pk_bf16_f32 v240, v116, v117
	v_cvt_pk_bf16_f32 v241, v118, v119
	ds_write_b64 v0, v[240:241]
	v_lshlrev_b32_e32 v168, 16, v30
	v_and_b32_e32 v169, 0xffff0000, v30
	v_lshlrev_b32_e32 v170, 16, v31
	v_and_b32_e32 v171, 0xffff0000, v31
	v_lshlrev_b32_e32 v172, 16, v32
	v_and_b32_e32 v173, 0xffff0000, v32
	v_lshlrev_b32_e32 v174, 16, v33
	v_and_b32_e32 v175, 0xffff0000, v33
	v_pk_mul_f32 v[168:169], v[4:5], v[168:169] op_sel_hi:[0,1]
	v_pk_mul_f32 v[170:171], v[4:5], v[170:171] op_sel_hi:[0,1]
	v_pk_fma_f32 v[112:113], v[184:185], v[112:113], v[168:169] op_sel_hi:[0,1,1]
	v_pk_fma_f32 v[114:115], v[184:185], v[114:115], v[170:171] op_sel_hi:[0,1,1]
	v_pk_mul_f32 v[112:113], v[112:113], v[172:173]
	v_pk_mul_f32 v[114:115], v[114:115], v[174:175]
	v_cvt_pk_bf16_f32 v240, v112, v113
	v_cvt_pk_bf16_f32 v241, v114, v115
	ds_write_b64 v0, v[240:241] offset:32
	v_lshlrev_b32_e32 v168, 16, v34
	v_and_b32_e32 v169, 0xffff0000, v34
	v_lshlrev_b32_e32 v170, 16, v35
	v_and_b32_e32 v171, 0xffff0000, v35
	v_lshlrev_b32_e32 v172, 16, v36
	v_and_b32_e32 v173, 0xffff0000, v36
	v_lshlrev_b32_e32 v174, 16, v37
	v_and_b32_e32 v175, 0xffff0000, v37
	v_pk_mul_f32 v[168:169], v[4:5], v[168:169] op_sel_hi:[0,1]
	v_pk_mul_f32 v[170:171], v[4:5], v[170:171] op_sel_hi:[0,1]
	v_pk_fma_f32 v[108:109], v[184:185], v[108:109], v[168:169] op_sel_hi:[0,1,1]
	v_pk_fma_f32 v[110:111], v[184:185], v[110:111], v[170:171] op_sel_hi:[0,1,1]
	v_pk_mul_f32 v[108:109], v[108:109], v[172:173]
	v_pk_mul_f32 v[110:111], v[110:111], v[174:175]
	v_cvt_pk_bf16_f32 v240, v108, v109
	v_cvt_pk_bf16_f32 v241, v110, v111
	ds_write_b64 v0, v[240:241] offset:64
	v_lshlrev_b32_e32 v168, 16, v236
	v_and_b32_e32 v169, 0xffff0000, v236
	v_lshlrev_b32_e32 v170, 16, v237
	v_and_b32_e32 v171, 0xffff0000, v237
	v_lshlrev_b32_e32 v172, 16, v238
	v_and_b32_e32 v173, 0xffff0000, v238
	v_lshlrev_b32_e32 v174, 16, v239
	v_and_b32_e32 v175, 0xffff0000, v239
	v_pk_mul_f32 v[168:169], v[4:5], v[168:169] op_sel_hi:[0,1]
	v_pk_mul_f32 v[170:171], v[4:5], v[170:171] op_sel_hi:[0,1]
	v_pk_fma_f32 v[104:105], v[184:185], v[104:105], v[168:169] op_sel_hi:[0,1,1]
	v_pk_fma_f32 v[106:107], v[184:185], v[106:107], v[170:171] op_sel_hi:[0,1,1]
	v_pk_mul_f32 v[104:105], v[104:105], v[172:173]
	v_pk_mul_f32 v[106:107], v[106:107], v[174:175]
	v_cvt_pk_bf16_f32 v240, v104, v105
	v_cvt_pk_bf16_f32 v241, v106, v107
	ds_write_b64 v0, v[240:241] offset:96
	ds_read_b128 v[168:171], v1
	ds_read_b128 v[172:175], v1 offset:1152
	s_cbranch_vccz .Lt8z_1_1
	v_med3_f32 v248, v116, s77, v252
	v_med3_f32 v249, v117, s77, v252
	v_med3_f32 v250, v118, s77, v252
	v_med3_f32 v251, v119, s77, v252
	v_mov_b32_e32 v246, v245
	v_cvt_pk_fp8_f32 v246, v248, v249
	v_cvt_pk_fp8_f32 v246, v250, v251 op_sel:[0,0,1]
	ds_write_b32 v38, v246 offset:64
	v_med3_f32 v248, v112, s77, v252
	v_med3_f32 v249, v113, s77, v252
	v_med3_f32 v250, v114, s77, v252
	v_med3_f32 v251, v115, s77, v252
	v_mov_b32_e32 v246, v245
	v_cvt_pk_fp8_f32 v246, v248, v249
	v_cvt_pk_fp8_f32 v246, v250, v251 op_sel:[0,0,1]
	ds_write_b32 v38, v246 offset:80
	v_med3_f32 v248, v108, s77, v252
	v_med3_f32 v249, v109, s77, v252
	v_med3_f32 v250, v110, s77, v252
	v_med3_f32 v251, v111, s77, v252
	v_mov_b32_e32 v246, v245
	v_cvt_pk_fp8_f32 v246, v248, v249
	v_cvt_pk_fp8_f32 v246, v250, v251 op_sel:[0,0,1]
	ds_write_b32 v38, v246 offset:96
	v_med3_f32 v248, v104, s77, v252
	v_med3_f32 v249, v105, s77, v252
	v_med3_f32 v250, v106, s77, v252
	v_med3_f32 v251, v107, s77, v252
	v_mov_b32_e32 v246, v245
	v_cvt_pk_fp8_f32 v246, v248, v249
	v_cvt_pk_fp8_f32 v246, v250, v251 op_sel:[0,0,1]
	ds_write_b32 v38, v246 offset:112
.Lt8z_1_1:
	s_waitcnt lgkmcnt(0)
	global_store_dwordx4 v[194:195], v[168:171], off offset:384
	global_store_dwordx4 v[196:197], v[172:175], off offset:384
	s_nop 1
	s_cbranch_vccz .Lt8zs_1
	ds_read_b128 v[168:171], v39
	ds_read_b128 v[172:175], v39 offset:1152
	s_waitcnt lgkmcnt(0)
	global_store_dwordx4 v[2:3], v[168:171], off offset:128
	global_store_dwordx4 v[198:199], v[172:175], off offset:128
	s_nop 1
.Lt8zs_1:
	global_load_dwordx2 v[10:11], v[8:9], off offset:768
	global_load_dwordx2 v[12:13], v[6:7], off offset:768
	global_load_dwordx2 v[14:15], v[8:9], off offset:800
	global_load_dwordx2 v[16:17], v[6:7], off offset:800
	global_load_dwordx2 v[18:19], v[8:9], off offset:832
	global_load_dwordx2 v[20:21], v[6:7], off offset:832
	global_load_dwordx2 v[22:23], v[8:9], off offset:864
	global_load_dwordx2 v[24:25], v[6:7], off offset:864
	global_load_dwordx2 v[26:27], v[8:9], off offset:896
	global_load_dwordx2 v[28:29], v[6:7], off offset:896
	global_load_dwordx2 v[30:31], v[8:9], off offset:928
	global_load_dwordx2 v[32:33], v[6:7], off offset:928
	global_load_dwordx2 v[34:35], v[8:9], off offset:960
	global_load_dwordx2 v[36:37], v[6:7], off offset:960
	global_load_dwordx2 v[236:237], v[8:9], off offset:992
	global_load_dwordx2 v[238:239], v[6:7], off offset:992
	s_waitcnt vmcnt(20)
	v_lshlrev_b32_e32 v168, 16, v204
	v_and_b32_e32 v169, 0xffff0000, v204
	v_lshlrev_b32_e32 v170, 16, v205
	v_and_b32_e32 v171, 0xffff0000, v205
	v_lshlrev_b32_e32 v172, 16, v206
	v_and_b32_e32 v173, 0xffff0000, v206
	v_lshlrev_b32_e32 v174, 16, v207
	v_and_b32_e32 v175, 0xffff0000, v207
	v_pk_mul_f32 v[168:169], v[4:5], v[168:169] op_sel_hi:[0,1]
	v_pk_mul_f32 v[170:171], v[4:5], v[170:171] op_sel_hi:[0,1]
	v_pk_fma_f32 v[100:101], v[184:185], v[100:101], v[168:169] op_sel_hi:[0,1,1]
	v_pk_fma_f32 v[102:103], v[184:185], v[102:103], v[170:171] op_sel_hi:[0,1,1]
	v_pk_mul_f32 v[100:101], v[100:101], v[172:173]
	v_pk_mul_f32 v[102:103], v[102:103], v[174:175]
	v_cvt_pk_bf16_f32 v240, v100, v101
	v_cvt_pk_bf16_f32 v241, v102, v103
	ds_write_b64 v0, v[240:241]
	v_lshlrev_b32_e32 v168, 16, v208
	v_and_b32_e32 v169, 0xffff0000, v208
	v_lshlrev_b32_e32 v170, 16, v209
	v_and_b32_e32 v171, 0xffff0000, v209
	v_lshlrev_b32_e32 v172, 16, v210
	v_and_b32_e32 v173, 0xffff0000, v210
	v_lshlrev_b32_e32 v174, 16, v211
	v_and_b32_e32 v175, 0xffff0000, v211
	v_pk_mul_f32 v[168:169], v[4:5], v[168:169] op_sel_hi:[0,1]
	v_pk_mul_f32 v[170:171], v[4:5], v[170:171] op_sel_hi:[0,1]
	v_pk_fma_f32 v[96:97], v[184:185], v[96:97], v[168:169] op_sel_hi:[0,1,1]
	v_pk_fma_f32 v[98:99], v[184:185], v[98:99], v[170:171] op_sel_hi:[0,1,1]
	v_pk_mul_f32 v[96:97], v[96:97], v[172:173]
	v_pk_mul_f32 v[98:99], v[98:99], v[174:175]
	v_cvt_pk_bf16_f32 v240, v96, v97
	v_cvt_pk_bf16_f32 v241, v98, v99
	ds_write_b64 v0, v[240:241] offset:32
	v_lshlrev_b32_e32 v168, 16, v212
	v_and_b32_e32 v169, 0xffff0000, v212
	v_lshlrev_b32_e32 v170, 16, v213
	v_and_b32_e32 v171, 0xffff0000, v213
	v_lshlrev_b32_e32 v172, 16, v214
	v_and_b32_e32 v173, 0xffff0000, v214
	v_lshlrev_b32_e32 v174, 16, v215
	v_and_b32_e32 v175, 0xffff0000, v215
	v_pk_mul_f32 v[168:169], v[4:5], v[168:169] op_sel_hi:[0,1]
	v_pk_mul_f32 v[170:171], v[4:5], v[170:171] op_sel_hi:[0,1]
	v_pk_fma_f32 v[92:93], v[184:185], v[92:93], v[168:169] op_sel_hi:[0,1,1]
	v_pk_fma_f32 v[94:95], v[184:185], v[94:95], v[170:171] op_sel_hi:[0,1,1]
	v_pk_mul_f32 v[92:93], v[92:93], v[172:173]
	v_pk_mul_f32 v[94:95], v[94:95], v[174:175]
	v_cvt_pk_bf16_f32 v240, v92, v93
	v_cvt_pk_bf16_f32 v241, v94, v95
	ds_write_b64 v0, v[240:241] offset:64
	v_lshlrev_b32_e32 v168, 16, v216
	v_and_b32_e32 v169, 0xffff0000, v216
	v_lshlrev_b32_e32 v170, 16, v217
	v_and_b32_e32 v171, 0xffff0000, v217
	v_lshlrev_b32_e32 v172, 16, v218
	v_and_b32_e32 v173, 0xffff0000, v218
	v_lshlrev_b32_e32 v174, 16, v219
	v_and_b32_e32 v175, 0xffff0000, v219
	v_pk_mul_f32 v[168:169], v[4:5], v[168:169] op_sel_hi:[0,1]
	v_pk_mul_f32 v[170:171], v[4:5], v[170:171] op_sel_hi:[0,1]
	v_pk_fma_f32 v[88:89], v[184:185], v[88:89], v[168:169] op_sel_hi:[0,1,1]
	v_pk_fma_f32 v[90:91], v[184:185], v[90:91], v[170:171] op_sel_hi:[0,1,1]
	v_pk_mul_f32 v[88:89], v[88:89], v[172:173]
	v_pk_mul_f32 v[90:91], v[90:91], v[174:175]
	v_cvt_pk_bf16_f32 v240, v88, v89
	v_cvt_pk_bf16_f32 v241, v90, v91
	ds_write_b64 v0, v[240:241] offset:96
	ds_read_b128 v[168:171], v1
	ds_read_b128 v[172:175], v1 offset:1152
	s_cbranch_vccz .Lt8z_2_0
	v_med3_f32 v248, v100, s77, v252
	v_med3_f32 v249, v101, s77, v252
	v_med3_f32 v250, v102, s77, v252
	v_med3_f32 v251, v103, s77, v252
	v_mov_b32_e32 v246, v245
	v_cvt_pk_fp8_f32 v246, v248, v249
	v_cvt_pk_fp8_f32 v246, v250, v251 op_sel:[0,0,1]
	ds_write_b32 v38, v246
	v_med3_f32 v248, v96, s77, v252
	v_med3_f32 v249, v97, s77, v252
	v_med3_f32 v250, v98, s77, v252
	v_med3_f32 v251, v99, s77, v252
	v_mov_b32_e32 v246, v245
	v_cvt_pk_fp8_f32 v246, v248, v249
	v_cvt_pk_fp8_f32 v246, v250, v251 op_sel:[0,0,1]
	ds_write_b32 v38, v246 offset:16
	v_med3_f32 v248, v92, s77, v252
	v_med3_f32 v249, v93, s77, v252
	v_med3_f32 v250, v94, s77, v252
	v_med3_f32 v251, v95, s77, v252
	v_mov_b32_e32 v246, v245
	v_cvt_pk_fp8_f32 v246, v248, v249
	v_cvt_pk_fp8_f32 v246, v250, v251 op_sel:[0,0,1]
	ds_write_b32 v38, v246 offset:32
	v_med3_f32 v248, v88, s77, v252
	v_med3_f32 v249, v89, s77, v252
	v_med3_f32 v250, v90, s77, v252
	v_med3_f32 v251, v91, s77, v252
	v_mov_b32_e32 v246, v245
	v_cvt_pk_fp8_f32 v246, v248, v249
	v_cvt_pk_fp8_f32 v246, v250, v251 op_sel:[0,0,1]
	ds_write_b32 v38, v246 offset:48
.Lt8z_2_0:
	s_waitcnt lgkmcnt(0)
	global_store_dwordx4 v[194:195], v[168:171], off offset:512
	global_store_dwordx4 v[196:197], v[172:175], off offset:512
	s_nop 1
	v_lshlrev_b32_e32 v168, 16, v220
	v_and_b32_e32 v169, 0xffff0000, v220
	v_lshlrev_b32_e32 v170, 16, v221
	v_and_b32_e32 v171, 0xffff0000, v221
	v_lshlrev_b32_e32 v172, 16, v222
	v_and_b32_e32 v173, 0xffff0000, v222
	v_lshlrev_b32_e32 v174, 16, v223
	v_and_b32_e32 v175, 0xffff0000, v223
	v_pk_mul_f32 v[168:169], v[4:5], v[168:169] op_sel_hi:[0,1]
	v_pk_mul_f32 v[170:171], v[4:5], v[170:171] op_sel_hi:[0,1]
	v_pk_fma_f32 v[84:85], v[184:185], v[84:85], v[168:169] op_sel_hi:[0,1,1]
	v_pk_fma_f32 v[86:87], v[184:185], v[86:87], v[170:171] op_sel_hi:[0,1,1]
	v_pk_mul_f32 v[84:85], v[84:85], v[172:173]
	v_pk_mul_f32 v[86:87], v[86:87], v[174:175]
	v_cvt_pk_bf16_f32 v240, v84, v85
	v_cvt_pk_bf16_f32 v241, v86, v87
	ds_write_b64 v0, v[240:241]
	v_lshlrev_b32_e32 v168, 16, v224
	v_and_b32_e32 v169, 0xffff0000, v224
	v_lshlrev_b32_e32 v170, 16, v225
	v_and_b32_e32 v171, 0xffff0000, v225
	v_lshlrev_b32_e32 v172, 16, v226
	v_and_b32_e32 v173, 0xffff0000, v226
	v_lshlrev_b32_e32 v174, 16, v227
	v_and_b32_e32 v175, 0xffff0000, v227
	v_pk_mul_f32 v[168:169], v[4:5], v[168:169] op_sel_hi:[0,1]
	v_pk_mul_f32 v[170:171], v[4:5], v[170:171] op_sel_hi:[0,1]
	v_pk_fma_f32 v[80:81], v[184:185], v[80:81], v[168:169] op_sel_hi:[0,1,1]
	v_pk_fma_f32 v[82:83], v[184:185], v[82:83], v[170:171] op_sel_hi:[0,1,1]
	v_pk_mul_f32 v[80:81], v[80:81], v[172:173]
	v_pk_mul_f32 v[82:83], v[82:83], v[174:175]
	v_cvt_pk_bf16_f32 v240, v80, v81
	v_cvt_pk_bf16_f32 v241, v82, v83
	ds_write_b64 v0, v[240:241] offset:32
	v_lshlrev_b32_e32 v168, 16, v228
	v_and_b32_e32 v169, 0xffff0000, v228
	v_lshlrev_b32_e32 v170, 16, v229
	v_and_b32_e32 v171, 0xffff0000, v229
	v_lshlrev_b32_e32 v172, 16, v230
	v_and_b32_e32 v173, 0xffff0000, v230
	v_lshlrev_b32_e32 v174, 16, v231
	v_and_b32_e32 v175, 0xffff0000, v231
	v_pk_mul_f32 v[168:169], v[4:5], v[168:169] op_sel_hi:[0,1]
	v_pk_mul_f32 v[170:171], v[4:5], v[170:171] op_sel_hi:[0,1]
	v_pk_fma_f32 v[76:77], v[184:185], v[76:77], v[168:169] op_sel_hi:[0,1,1]
	v_pk_fma_f32 v[78:79], v[184:185], v[78:79], v[170:171] op_sel_hi:[0,1,1]
	v_pk_mul_f32 v[76:77], v[76:77], v[172:173]
	v_pk_mul_f32 v[78:79], v[78:79], v[174:175]
	v_cvt_pk_bf16_f32 v240, v76, v77
	v_cvt_pk_bf16_f32 v241, v78, v79
	ds_write_b64 v0, v[240:241] offset:64
	v_lshlrev_b32_e32 v168, 16, v232
	v_and_b32_e32 v169, 0xffff0000, v232
	v_lshlrev_b32_e32 v170, 16, v233
	v_and_b32_e32 v171, 0xffff0000, v233
	v_lshlrev_b32_e32 v172, 16, v234
	v_and_b32_e32 v173, 0xffff0000, v234
	v_lshlrev_b32_e32 v174, 16, v235
	v_and_b32_e32 v175, 0xffff0000, v235
	v_pk_mul_f32 v[168:169], v[4:5], v[168:169] op_sel_hi:[0,1]
	v_pk_mul_f32 v[170:171], v[4:5], v[170:171] op_sel_hi:[0,1]
	v_pk_fma_f32 v[72:73], v[184:185], v[72:73], v[168:169] op_sel_hi:[0,1,1]
	v_pk_fma_f32 v[74:75], v[184:185], v[74:75], v[170:171] op_sel_hi:[0,1,1]
	v_pk_mul_f32 v[72:73], v[72:73], v[172:173]
	v_pk_mul_f32 v[74:75], v[74:75], v[174:175]
	v_cvt_pk_bf16_f32 v240, v72, v73
	v_cvt_pk_bf16_f32 v241, v74, v75
	ds_write_b64 v0, v[240:241] offset:96
	ds_read_b128 v[168:171], v1
	ds_read_b128 v[172:175], v1 offset:1152
	s_cbranch_vccz .Lt8z_2_1
	v_med3_f32 v248, v84, s77, v252
	v_med3_f32 v249, v85, s77, v252
	v_med3_f32 v250, v86, s77, v252
	v_med3_f32 v251, v87, s77, v252
	v_mov_b32_e32 v246, v245
	v_cvt_pk_fp8_f32 v246, v248, v249
	v_cvt_pk_fp8_f32 v246, v250, v251 op_sel:[0,0,1]
	ds_write_b32 v38, v246 offset:64
	v_med3_f32 v248, v80, s77, v252
	v_med3_f32 v249, v81, s77, v252
	v_med3_f32 v250, v82, s77, v252
	v_med3_f32 v251, v83, s77, v252
	v_mov_b32_e32 v246, v245
	v_cvt_pk_fp8_f32 v246, v248, v249
	v_cvt_pk_fp8_f32 v246, v250, v251 op_sel:[0,0,1]
	ds_write_b32 v38, v246 offset:80
	v_med3_f32 v248, v76, s77, v252
	v_med3_f32 v249, v77, s77, v252
	v_med3_f32 v250, v78, s77, v252
	v_med3_f32 v251, v79, s77, v252
	v_mov_b32_e32 v246, v245
	v_cvt_pk_fp8_f32 v246, v248, v249
	v_cvt_pk_fp8_f32 v246, v250, v251 op_sel:[0,0,1]
	ds_write_b32 v38, v246 offset:96
	v_med3_f32 v248, v72, s77, v252
	v_med3_f32 v249, v73, s77, v252
	v_med3_f32 v250, v74, s77, v252
	v_med3_f32 v251, v75, s77, v252
	v_mov_b32_e32 v246, v245
	v_cvt_pk_fp8_f32 v246, v248, v249
	v_cvt_pk_fp8_f32 v246, v250, v251 op_sel:[0,0,1]
	ds_write_b32 v38, v246 offset:112
.Lt8z_2_1:
	s_waitcnt lgkmcnt(0)
	global_store_dwordx4 v[194:195], v[168:171], off offset:640
	global_store_dwordx4 v[196:197], v[172:175], off offset:640
	s_nop 1
	s_cbranch_vccz .Lt8zs_2
	ds_read_b128 v[168:171], v39
	ds_read_b128 v[172:175], v39 offset:1152
	s_waitcnt lgkmcnt(0)
	global_store_dwordx4 v[2:3], v[168:171], off offset:256
	global_store_dwordx4 v[198:199], v[172:175], off offset:256
	s_nop 1
.Lt8zs_2:
	s_waitcnt vmcnt(4)
	v_lshlrev_b32_e32 v168, 16, v10
	v_and_b32_e32 v169, 0xffff0000, v10
	v_lshlrev_b32_e32 v170, 16, v11
	v_and_b32_e32 v171, 0xffff0000, v11
	v_lshlrev_b32_e32 v172, 16, v12
	v_and_b32_e32 v173, 0xffff0000, v12
	v_lshlrev_b32_e32 v174, 16, v13
	v_and_b32_e32 v175, 0xffff0000, v13
	v_pk_mul_f32 v[168:169], v[4:5], v[168:169] op_sel_hi:[0,1]
	v_pk_mul_f32 v[170:171], v[4:5], v[170:171] op_sel_hi:[0,1]
	v_pk_fma_f32 v[68:69], v[184:185], v[68:69], v[168:169] op_sel_hi:[0,1,1]
	v_pk_fma_f32 v[70:71], v[184:185], v[70:71], v[170:171] op_sel_hi:[0,1,1]
	v_pk_mul_f32 v[68:69], v[68:69], v[172:173]
	v_pk_mul_f32 v[70:71], v[70:71], v[174:175]
	v_cvt_pk_bf16_f32 v240, v68, v69
	v_cvt_pk_bf16_f32 v241, v70, v71
	ds_write_b64 v0, v[240:241]
	v_lshlrev_b32_e32 v168, 16, v14
	v_and_b32_e32 v169, 0xffff0000, v14
	v_lshlrev_b32_e32 v170, 16, v15
	v_and_b32_e32 v171, 0xffff0000, v15
	v_lshlrev_b32_e32 v172, 16, v16
	v_and_b32_e32 v173, 0xffff0000, v16
	v_lshlrev_b32_e32 v174, 16, v17
	v_and_b32_e32 v175, 0xffff0000, v17
	v_pk_mul_f32 v[168:169], v[4:5], v[168:169] op_sel_hi:[0,1]
	v_pk_mul_f32 v[170:171], v[4:5], v[170:171] op_sel_hi:[0,1]
	v_pk_fma_f32 v[64:65], v[184:185], v[64:65], v[168:169] op_sel_hi:[0,1,1]
	v_pk_fma_f32 v[66:67], v[184:185], v[66:67], v[170:171] op_sel_hi:[0,1,1]
	v_pk_mul_f32 v[64:65], v[64:65], v[172:173]
	v_pk_mul_f32 v[66:67], v[66:67], v[174:175]
	v_cvt_pk_bf16_f32 v240, v64, v65
	v_cvt_pk_bf16_f32 v241, v66, v67
	ds_write_b64 v0, v[240:241] offset:32
	v_lshlrev_b32_e32 v168, 16, v18
	v_and_b32_e32 v169, 0xffff0000, v18
	v_lshlrev_b32_e32 v170, 16, v19
	v_and_b32_e32 v171, 0xffff0000, v19
	v_lshlrev_b32_e32 v172, 16, v20
	v_and_b32_e32 v173, 0xffff0000, v20
	v_lshlrev_b32_e32 v174, 16, v21
	v_and_b32_e32 v175, 0xffff0000, v21
	v_pk_mul_f32 v[168:169], v[4:5], v[168:169] op_sel_hi:[0,1]
	v_pk_mul_f32 v[170:171], v[4:5], v[170:171] op_sel_hi:[0,1]
	v_pk_fma_f32 v[60:61], v[184:185], v[60:61], v[168:169] op_sel_hi:[0,1,1]
	v_pk_fma_f32 v[62:63], v[184:185], v[62:63], v[170:171] op_sel_hi:[0,1,1]
	v_pk_mul_f32 v[60:61], v[60:61], v[172:173]
	v_pk_mul_f32 v[62:63], v[62:63], v[174:175]
	v_cvt_pk_bf16_f32 v240, v60, v61
	v_cvt_pk_bf16_f32 v241, v62, v63
	ds_write_b64 v0, v[240:241] offset:64
	v_lshlrev_b32_e32 v168, 16, v22
	v_and_b32_e32 v169, 0xffff0000, v22
	v_lshlrev_b32_e32 v170, 16, v23
	v_and_b32_e32 v171, 0xffff0000, v23
	v_lshlrev_b32_e32 v172, 16, v24
	v_and_b32_e32 v173, 0xffff0000, v24
	v_lshlrev_b32_e32 v174, 16, v25
	v_and_b32_e32 v175, 0xffff0000, v25
	v_pk_mul_f32 v[168:169], v[4:5], v[168:169] op_sel_hi:[0,1]
	v_pk_mul_f32 v[170:171], v[4:5], v[170:171] op_sel_hi:[0,1]
	v_pk_fma_f32 v[56:57], v[184:185], v[56:57], v[168:169] op_sel_hi:[0,1,1]
	v_pk_fma_f32 v[58:59], v[184:185], v[58:59], v[170:171] op_sel_hi:[0,1,1]
	v_pk_mul_f32 v[56:57], v[56:57], v[172:173]
	v_pk_mul_f32 v[58:59], v[58:59], v[174:175]
	v_cvt_pk_bf16_f32 v240, v56, v57
	v_cvt_pk_bf16_f32 v241, v58, v59
	ds_write_b64 v0, v[240:241] offset:96
	ds_read_b128 v[168:171], v1
	ds_read_b128 v[172:175], v1 offset:1152
	s_cbranch_vccz .Lt8z_3_0
	v_med3_f32 v248, v68, s77, v252
	v_med3_f32 v249, v69, s77, v252
	v_med3_f32 v250, v70, s77, v252
	v_med3_f32 v251, v71, s77, v252
	v_mov_b32_e32 v246, v245
	v_cvt_pk_fp8_f32 v246, v248, v249
	v_cvt_pk_fp8_f32 v246, v250, v251 op_sel:[0,0,1]
	ds_write_b32 v38, v246
	v_med3_f32 v248, v64, s77, v252
	v_med3_f32 v249, v65, s77, v252
	v_med3_f32 v250, v66, s77, v252
	v_med3_f32 v251, v67, s77, v252
	v_mov_b32_e32 v246, v245
	v_cvt_pk_fp8_f32 v246, v248, v249
	v_cvt_pk_fp8_f32 v246, v250, v251 op_sel:[0,0,1]
	ds_write_b32 v38, v246 offset:16
	v_med3_f32 v248, v60, s77, v252
	v_med3_f32 v249, v61, s77, v252
	v_med3_f32 v250, v62, s77, v252
	v_med3_f32 v251, v63, s77, v252
	v_mov_b32_e32 v246, v245
	v_cvt_pk_fp8_f32 v246, v248, v249
	v_cvt_pk_fp8_f32 v246, v250, v251 op_sel:[0,0,1]
	ds_write_b32 v38, v246 offset:32
	v_med3_f32 v248, v56, s77, v252
	v_med3_f32 v249, v57, s77, v252
	v_med3_f32 v250, v58, s77, v252
	v_med3_f32 v251, v59, s77, v252
	v_mov_b32_e32 v246, v245
	v_cvt_pk_fp8_f32 v246, v248, v249
	v_cvt_pk_fp8_f32 v246, v250, v251 op_sel:[0,0,1]
	ds_write_b32 v38, v246 offset:48
.Lt8z_3_0:
	s_waitcnt lgkmcnt(0)
	global_store_dwordx4 v[194:195], v[168:171], off offset:768
	global_store_dwordx4 v[196:197], v[172:175], off offset:768
	s_nop 1
	v_lshlrev_b32_e32 v168, 16, v26
	v_and_b32_e32 v169, 0xffff0000, v26
	v_lshlrev_b32_e32 v170, 16, v27
	v_and_b32_e32 v171, 0xffff0000, v27
	v_lshlrev_b32_e32 v172, 16, v28
	v_and_b32_e32 v173, 0xffff0000, v28
	v_lshlrev_b32_e32 v174, 16, v29
	v_and_b32_e32 v175, 0xffff0000, v29
	v_pk_mul_f32 v[168:169], v[4:5], v[168:169] op_sel_hi:[0,1]
	v_pk_mul_f32 v[170:171], v[4:5], v[170:171] op_sel_hi:[0,1]
	v_pk_fma_f32 v[52:53], v[184:185], v[52:53], v[168:169] op_sel_hi:[0,1,1]
	v_pk_fma_f32 v[54:55], v[184:185], v[54:55], v[170:171] op_sel_hi:[0,1,1]
	v_pk_mul_f32 v[52:53], v[52:53], v[172:173]
	v_pk_mul_f32 v[54:55], v[54:55], v[174:175]
	v_cvt_pk_bf16_f32 v240, v52, v53
	v_cvt_pk_bf16_f32 v241, v54, v55
	ds_write_b64 v0, v[240:241]
	v_lshlrev_b32_e32 v168, 16, v30
	v_and_b32_e32 v169, 0xffff0000, v30
	v_lshlrev_b32_e32 v170, 16, v31
	v_and_b32_e32 v171, 0xffff0000, v31
	v_lshlrev_b32_e32 v172, 16, v32
	v_and_b32_e32 v173, 0xffff0000, v32
	v_lshlrev_b32_e32 v174, 16, v33
	v_and_b32_e32 v175, 0xffff0000, v33
	v_pk_mul_f32 v[168:169], v[4:5], v[168:169] op_sel_hi:[0,1]
	v_pk_mul_f32 v[170:171], v[4:5], v[170:171] op_sel_hi:[0,1]
	v_pk_fma_f32 v[48:49], v[184:185], v[48:49], v[168:169] op_sel_hi:[0,1,1]
	v_pk_fma_f32 v[50:51], v[184:185], v[50:51], v[170:171] op_sel_hi:[0,1,1]
	v_pk_mul_f32 v[48:49], v[48:49], v[172:173]
	v_pk_mul_f32 v[50:51], v[50:51], v[174:175]
	v_cvt_pk_bf16_f32 v240, v48, v49
	v_cvt_pk_bf16_f32 v241, v50, v51
	ds_write_b64 v0, v[240:241] offset:32
	v_lshlrev_b32_e32 v168, 16, v34
	v_and_b32_e32 v169, 0xffff0000, v34
	v_lshlrev_b32_e32 v170, 16, v35
	v_and_b32_e32 v171, 0xffff0000, v35
	v_lshlrev_b32_e32 v172, 16, v36
	v_and_b32_e32 v173, 0xffff0000, v36
	v_lshlrev_b32_e32 v174, 16, v37
	v_and_b32_e32 v175, 0xffff0000, v37
	v_pk_mul_f32 v[168:169], v[4:5], v[168:169] op_sel_hi:[0,1]
	v_pk_mul_f32 v[170:171], v[4:5], v[170:171] op_sel_hi:[0,1]
	v_pk_fma_f32 v[44:45], v[184:185], v[44:45], v[168:169] op_sel_hi:[0,1,1]
	v_pk_fma_f32 v[46:47], v[184:185], v[46:47], v[170:171] op_sel_hi:[0,1,1]
	v_pk_mul_f32 v[44:45], v[44:45], v[172:173]
	v_pk_mul_f32 v[46:47], v[46:47], v[174:175]
	v_cvt_pk_bf16_f32 v240, v44, v45
	v_cvt_pk_bf16_f32 v241, v46, v47
	ds_write_b64 v0, v[240:241] offset:64
	v_lshlrev_b32_e32 v168, 16, v236
	v_and_b32_e32 v169, 0xffff0000, v236
	v_lshlrev_b32_e32 v170, 16, v237
	v_and_b32_e32 v171, 0xffff0000, v237
	v_lshlrev_b32_e32 v172, 16, v238
	v_and_b32_e32 v173, 0xffff0000, v238
	v_lshlrev_b32_e32 v174, 16, v239
	v_and_b32_e32 v175, 0xffff0000, v239
	v_pk_mul_f32 v[168:169], v[4:5], v[168:169] op_sel_hi:[0,1]
	v_pk_mul_f32 v[170:171], v[4:5], v[170:171] op_sel_hi:[0,1]
	v_pk_fma_f32 v[40:41], v[184:185], v[40:41], v[168:169] op_sel_hi:[0,1,1]
	v_pk_fma_f32 v[42:43], v[184:185], v[42:43], v[170:171] op_sel_hi:[0,1,1]
	v_pk_mul_f32 v[40:41], v[40:41], v[172:173]
	v_pk_mul_f32 v[42:43], v[42:43], v[174:175]
	v_cvt_pk_bf16_f32 v240, v40, v41
	v_cvt_pk_bf16_f32 v241, v42, v43
	ds_write_b64 v0, v[240:241] offset:96
	ds_read_b128 v[168:171], v1
	ds_read_b128 v[172:175], v1 offset:1152
	s_cbranch_vccz .Lt8z_3_1
	v_med3_f32 v248, v52, s77, v252
	v_med3_f32 v249, v53, s77, v252
	v_med3_f32 v250, v54, s77, v252
	v_med3_f32 v251, v55, s77, v252
	v_mov_b32_e32 v246, v245
	v_cvt_pk_fp8_f32 v246, v248, v249
	v_cvt_pk_fp8_f32 v246, v250, v251 op_sel:[0,0,1]
	ds_write_b32 v38, v246 offset:64
	v_med3_f32 v248, v48, s77, v252
	v_med3_f32 v249, v49, s77, v252
	v_med3_f32 v250, v50, s77, v252
	v_med3_f32 v251, v51, s77, v252
	v_mov_b32_e32 v246, v245
	v_cvt_pk_fp8_f32 v246, v248, v249
	v_cvt_pk_fp8_f32 v246, v250, v251 op_sel:[0,0,1]
	ds_write_b32 v38, v246 offset:80
	v_med3_f32 v248, v44, s77, v252
	v_med3_f32 v249, v45, s77, v252
	v_med3_f32 v250, v46, s77, v252
	v_med3_f32 v251, v47, s77, v252
	v_mov_b32_e32 v246, v245
	v_cvt_pk_fp8_f32 v246, v248, v249
	v_cvt_pk_fp8_f32 v246, v250, v251 op_sel:[0,0,1]
	ds_write_b32 v38, v246 offset:96
	v_med3_f32 v248, v40, s77, v252
	v_med3_f32 v249, v41, s77, v252
	v_med3_f32 v250, v42, s77, v252
	v_med3_f32 v251, v43, s77, v252
	v_mov_b32_e32 v246, v245
	v_cvt_pk_fp8_f32 v246, v248, v249
	v_cvt_pk_fp8_f32 v246, v250, v251 op_sel:[0,0,1]
	ds_write_b32 v38, v246 offset:112
.Lt8z_3_1:
	s_waitcnt lgkmcnt(0)
	global_store_dwordx4 v[194:195], v[168:171], off offset:896
	global_store_dwordx4 v[196:197], v[172:175], off offset:896
	s_nop 1
	s_cbranch_vccz .Lt8zs_3
	ds_read_b128 v[168:171], v39
	ds_read_b128 v[172:175], v39 offset:1152
	s_waitcnt lgkmcnt(0)
	global_store_dwordx4 v[2:3], v[168:171], off offset:384
	global_store_dwordx4 v[198:199], v[172:175], off offset:384
	s_nop 1
